# v13 variant: FFT phase keeps 72 steps, gate/up GEMM of layer 0 piggybacks every other iteration
# baseline (speedup 1.0000x reference)
; __device__ __forceinline__ int tid_fresh() { int t = threadIdx.x; asm volatile("" : "+v"(t)); return t; }
; __device__ __forceinline__ unsigned cvt_pk_bf16(float lo, float hi) { unsigned r; asm volatile("v_cvt_pk_bf16_f32 %0, %1, %2" : "=v"(r) : "v"(lo), "v"(hi)); return r; }
; __device__ __forceinline__ bool bg_decode(int st, int wg, int NW, int lane, KP kp, const float*& src, int& ldS, bf16_t*& dst, int& o2) {
;     const int g = st * NW + wg;
;     if (g >= BG_STEPS) { src = kp->in[27] + lane; ldS = 0; dst = nullptr; o2 = 0; return false; }
; __device__ __forceinline__ void hy_fft_phase(LAS unsigned char* lds, int bid, int G, const bf16_t* vgT, bf16_t* zT, const float* a3, const float* wout, const float* skip, float* filt, float4* gspec) {
;     ...
;             const int tid = tid_fresh(), lane = tid & 63, wave = tid >> 6, col = lane & 15, kc = lane >> 4;
;             const int ci = g0 + (col >> 1), c = bid + G * ci; const bool cok = ci < nch;
;             bf16x8 bw[2];
; #pragma unroll
;             for (int ks = 0; ks < 2; ++ks) { float wv[8];
; #pragma unroll
;                 for (int q = 0; q < 8; ++q) wv[q] = wout[(size_t)(ks * 32 + kc * 8 + q) * 4096 + (col & 1) * D + (cok ? c : bid)] * (cok ? 1.f : 0.f);
;                 u32x4 w; w.x = cvt_pk_bf16(wv[0], wv[1]); w.y = cvt_pk_bf16(wv[2], wv[3]); w.z = cvt_pk_bf16(wv[4], wv[5]); w.w = cvt_pk_bf16(wv[6], wv[7]);
;                 bw[ks] = __builtin_bit_cast(bf16x8, w); }
.LBB0_377:
	v_mov_b32_e32 v14, v0
	v_readlane_b32 s0, v254, 4
	v_bfe_u32 v2, v14, 1, 3
	v_or_b32_e32 v2, s84, v2
	v_mul_lo_u32 v3, v2, s0
	v_readlane_b32 s0, v254, 19
	v_cmp_gt_i32_e32 vcc, s61, v2
	v_lshlrev_b32_e32 v4, 13, v14
	v_add_u32_e32 v16, s0, v3
	v_cndmask_b32_e32 v2, v63, v16, vcc
	v_and_b32_e32 v60, 0x2000, v4
	v_bfe_u32 v15, v14, 4, 2
	v_ashrrev_i32_e32 v3, 31, v2
	v_lshl_add_u64 v[4:5], s[4:5], 0, v[60:61]
	v_lshl_add_u64 v[2:3], v[2:3], 2, v[4:5]
	v_lshlrev_b32_e32 v60, 17, v15
	v_readlane_b32 s1, v254, 20
	v_lshl_add_u64 v[6:7], v[2:3], 0, v[60:61]
	s_movk_i32 s0, 0x4000
	v_add_co_u32_e64 v2, s[0:1], s0, v6
	v_cndmask_b32_e64 v29, 0, 1.0, vcc
	s_nop 0
	v_addc_co_u32_e64 v3, s[0:1], 0, v7, s[0:1]
	s_mov_b32 s0, 0x8000
	s_nop 0
	v_add_co_u32_e64 v4, s[0:1], s0, v6
	s_mul_i32 s28, s60, s16
	s_nop 0
	v_addc_co_u32_e64 v5, s[0:1], 0, v7, s[0:1]
	s_mov_b32 s0, 0xc000
	s_nop 0
	v_add_co_u32_e64 v8, s[0:1], s0, v6
	s_add_i32 s28, s28, s17
	s_nop 0
	v_addc_co_u32_e64 v9, s[0:1], 0, v7, s[0:1]
	v_add_co_u32_e64 v10, s[0:1], s71, v6
	s_cmp_gt_i32 s28, 0x23fff
	s_nop 0
	v_addc_co_u32_e64 v11, s[0:1], 0, v7, s[0:1]
	v_add_co_u32_e64 v12, s[0:1], s72, v6
	s_mov_b64 s[8:9], -1
	s_nop 0
	v_addc_co_u32_e64 v13, s[0:1], 0, v7, s[0:1]
	v_add_co_u32_e64 v18, s[0:1], s73, v6
	s_nop 1
	v_addc_co_u32_e64 v19, s[0:1], 0, v7, s[0:1]
	v_add_co_u32_e64 v20, s[0:1], s74, v6
	s_nop 1
	v_addc_co_u32_e64 v21, s[0:1], 0, v7, s[0:1]
	global_load_dword v17, v[6:7], off nt
	s_nop 0
	global_load_dword v2, v[2:3], off nt
	s_nop 0
	global_load_dword v3, v[4:5], off nt
	s_nop 0
	global_load_dword v4, v[8:9], off nt
	global_load_dword v5, v[10:11], off nt
	global_load_dword v26, v[12:13], off nt
	global_load_dword v27, v[18:19], off nt
	global_load_dword v28, v[20:21], off nt
	s_mov_b32 s0, 0x80000
	v_add_co_u32_e32 v8, vcc, s0, v6
	s_mov_b32 s0, 0x84000
	s_nop 0
	v_addc_co_u32_e32 v9, vcc, 0, v7, vcc
	v_add_co_u32_e32 v10, vcc, s0, v6
	s_mov_b32 s0, 0x88000
	s_nop 0
	v_addc_co_u32_e32 v11, vcc, 0, v7, vcc
	v_add_co_u32_e32 v12, vcc, s0, v6
	s_mov_b32 s0, 0x8c000
	s_nop 0
	v_addc_co_u32_e32 v13, vcc, 0, v7, vcc
	v_add_co_u32_e32 v18, vcc, s0, v6
	s_mov_b32 s0, 0x90000
	s_nop 0
	v_addc_co_u32_e32 v19, vcc, 0, v7, vcc
	v_add_co_u32_e32 v20, vcc, s0, v6
	s_mov_b32 s0, 0x94000
	s_nop 0
	v_addc_co_u32_e32 v21, vcc, 0, v7, vcc
	v_add_co_u32_e32 v22, vcc, s0, v6
	s_mov_b32 s0, 0x98000
	s_nop 0
	v_addc_co_u32_e32 v23, vcc, 0, v7, vcc
	v_add_co_u32_e32 v24, vcc, s0, v6
	s_mov_b32 s0, 0x9c000
	s_nop 0
	v_addc_co_u32_e32 v25, vcc, 0, v7, vcc
	v_add_co_u32_e32 v6, vcc, s0, v6
	v_readlane_b32 s0, v254, 0
	s_nop 0
	v_addc_co_u32_e32 v7, vcc, 0, v7, vcc
	v_readlane_b32 s1, v254, 1
	s_waitcnt vmcnt(7)
	v_mul_f32_e32 v17, v17, v29
	s_waitcnt vmcnt(6)
	v_mul_f32_e32 v2, v2, v29
	s_waitcnt vmcnt(5)
	v_mul_f32_e32 v3, v3, v29
	s_waitcnt vmcnt(4)
	v_mul_f32_e32 v4, v4, v29
	s_waitcnt vmcnt(3)
	v_mul_f32_e32 v5, v29, v5
	s_waitcnt vmcnt(2)
	v_mul_f32_e32 v26, v29, v26
	s_waitcnt vmcnt(1)
	v_mul_f32_e32 v27, v29, v27
	s_waitcnt vmcnt(0)
	v_mul_f32_e32 v28, v29, v28
	v_cvt_pk_bf16_f32 v2, v17, v2
	v_cvt_pk_bf16_f32 v3, v3, v4
	v_cvt_pk_bf16_f32 v4, v5, v26
	v_cvt_pk_bf16_f32 v5, v27, v28
	global_load_dword v8, v[8:9], off nt
	s_nop 0
	global_load_dword v9, v[10:11], off nt
	s_nop 0
	global_load_dword v10, v[12:13], off nt
	global_load_dword v11, v[18:19], off nt
	s_nop 0
	global_load_dword v12, v[20:21], off nt
	global_load_dword v13, v[22:23], off nt
	global_load_dword v17, v[24:25], off nt
	s_nop 0
	global_load_dword v6, v[6:7], off nt
	s_waitcnt vmcnt(7)
	v_mul_f32_e32 v7, v29, v8
	s_waitcnt vmcnt(6)
	v_mul_f32_e32 v8, v29, v9
	s_waitcnt vmcnt(5)
	v_mul_f32_e32 v9, v29, v10
	s_waitcnt vmcnt(4)
	v_mul_f32_e32 v10, v29, v11
	s_waitcnt vmcnt(3)
	v_mul_f32_e32 v11, v29, v12
	s_waitcnt vmcnt(2)
	v_mul_f32_e32 v12, v29, v13
	s_waitcnt vmcnt(1)
	v_mul_f32_e32 v13, v29, v17
	s_waitcnt vmcnt(0)
	v_mul_f32_e32 v17, v29, v6
	v_cvt_pk_bf16_f32 v6, v7, v8
	v_cvt_pk_bf16_f32 v7, v9, v10
	v_cvt_pk_bf16_f32 v8, v11, v12
	v_cvt_pk_bf16_f32 v9, v13, v17
	s_barrier
	s_cbranch_scc0 .LBB0_379
	s_load_dwordx2 s[8:9], s[0:1], 0xd8
	v_mov_b32_e32 v65, v61
	s_waitcnt lgkmcnt(0)
	v_lshl_add_u64 v[10:11], s[8:9], 0, v[64:65]
	s_mov_b64 s[8:9], 0

; __device__ __forceinline__ bool bg_decode(int st, int wg, int NW, int lane, KP kp, const float*& src, int& ldS, bf16_t*& dst, int& o2) {
;     const int g = st * NW + wg;
;     if (g >= BG_STEPS) { src = kp->in[27] + lane; ldS = 0; dst = nullptr; o2 = 0; return false; }
.LBB0_389:
	v_readlane_b32 s0, v254, 0
	s_add_i32 s33, s28, s53
	v_readlane_b32 s1, v254, 1
	s_cmp_lt_i32 s33, 0x24000
	s_mov_b64 s[42:43], -1
	s_cbranch_scc1 .LBB0_391
	s_load_dwordx2 s[42:43], s[0:1], 0xd8
	v_mov_b32_e32 v65, v61
	s_waitcnt lgkmcnt(0)
	v_lshl_add_u64 v[10:11], s[42:43], 0, v[64:65]
	s_mov_b64 s[42:43], 0

; __device__ __forceinline__ bool bg_decode(int st, int wg, int NW, int lane, KP kp, const float*& src, int& ldS, bf16_t*& dst, int& o2) {
;     const int g = st * NW + wg;
;     if (g >= BG_STEPS) { src = kp->in[27] + lane; ldS = 0; dst = nullptr; o2 = 0; return false; }
.LBB0_465:
	s_or_b64 exec, exec, s[42:43]
	v_readlane_b32 s42, v254, 0
	s_add_i32 s1, s49, s53
	v_readlane_b32 s43, v254, 1
	s_cmp_lt_i32 s1, 0x24000
	s_mov_b64 s[44:45], -1
	s_cbranch_scc1 .LBB0_467
	s_load_dwordx2 s[44:45], s[42:43], 0xd8
	v_mov_b32_e32 v65, v61
	s_waitcnt lgkmcnt(0)
	v_lshl_add_u64 v[10:11], s[44:45], 0, v[64:65]
	s_mov_b64 s[44:45], 0

; #define SEG_LD32(dst, off, base) asm volatile("global_load_dword %0, %1, %2" : "=v"(dst) : "v"(off), "s"(base) : "memory")
; #define BG_I(x) bg_issue1<x>(bg, bgwg, bgNW, bglane)
; __device__ __forceinline__ bool bg_decode(int st, int wg, int NW, int lane, KP kp, const float*& src, int& ldS, bf16_t*& dst, int& o2) {
;     const int g = st * NW + wg;
;     if (g >= BG_STEPS) { src = kp->in[27] + lane; ldS = 0; dst = nullptr; o2 = 0; return false; }
; __device__ __forceinline__ void hy_fft_phase(LAS unsigned char* lds, int bid, int G, const bf16_t* vgT, bf16_t* zT, const float* a3, const float* wout, const float* skip, float* filt, float4* gspec) {
;     ...
;             {   unsigned pa[16], pb[16]; float sk[2];
;                 const float* skp = skip; asm volatile("" : "+s"(skp));
; #pragma unroll
;                 for (int i = 0; i < 16; ++i) { const unsigned off = 4u * tid + 2048u * i; SEG_LD32(pa[i], off, A1); SEG_LD32(pb[i], off, A2); }
;                 { const unsigned o1 = 4u * c1, o2 = 4u * c2; SEG_LD32(sk[0], o1, skp); SEG_LD32(sk[1], o2, skp); }
;                 BG_I(1);
.LBB0_543:
	s_or_b32 s0, s87, 1
	v_readlane_b32 s1, v254, 4
	s_cmp_lt_i32 s0, s61
	s_mul_i32 s0, s87, s1
	v_readlane_b32 s42, v254, 19
	s_cselect_b64 s[8:9], -1, 0
	s_add_i32 s0, s0, s42
	v_readlane_b32 s43, v254, 20
	s_add_i32 s1, s0, s1
	s_and_b64 s[42:43], s[8:9], exec
	s_cselect_b32 s28, 0x8000, 0
	s_cselect_b32 s46, s1, s0
	s_sub_i32 s12, s87, s84
	s_lshl_b64 s[42:43], s[12:13], 15
	s_add_u32 s42, s10, s42
	s_addc_u32 s43, s11, s43
	v_mov_b32_e32 v80, v0
	s_mov_b64 s[50:51], s[6:7]
	s_add_u32 s48, s42, s28
	s_barrier
	s_addc_u32 s49, s43, 0
	v_lshlrev_b32_e32 v2, 2, v80
	global_load_dword v81, v2, s[42:43]
	global_load_dword v82, v2, s[48:49]
	v_add_u32_e32 v3, 0x800, v2
	global_load_dword v78, v3, s[42:43]
	global_load_dword v79, v3, s[48:49]
	v_add_u32_e32 v3, 0x1000, v2
	global_load_dword v76, v3, s[42:43]
	global_load_dword v77, v3, s[48:49]
	v_add_u32_e32 v3, 0x1800, v2
	global_load_dword v74, v3, s[42:43]
	global_load_dword v75, v3, s[48:49]
	v_add_u32_e32 v3, 0x2000, v2
	global_load_dword v72, v3, s[42:43]
	global_load_dword v73, v3, s[48:49]
	v_add_u32_e32 v3, 0x2800, v2
	global_load_dword v70, v3, s[42:43]
	global_load_dword v71, v3, s[48:49]
	v_add_u32_e32 v3, 0x3000, v2
	global_load_dword v56, v3, s[42:43]
	global_load_dword v57, v3, s[48:49]
	v_add_u32_e32 v3, 0x3800, v2
	global_load_dword v54, v3, s[42:43]
	global_load_dword v55, v3, s[48:49]
	v_add_u32_e32 v3, 0x4000, v2
	global_load_dword v52, v3, s[42:43]
	global_load_dword v53, v3, s[48:49]
	v_add_u32_e32 v3, 0x4800, v2
	global_load_dword v50, v3, s[42:43]
	global_load_dword v51, v3, s[48:49]
	v_add_u32_e32 v3, 0x5000, v2
	global_load_dword v48, v3, s[42:43]
	global_load_dword v49, v3, s[48:49]
	v_add_u32_e32 v3, 0x5800, v2
	global_load_dword v46, v3, s[42:43]
	global_load_dword v47, v3, s[48:49]
	v_add_u32_e32 v3, 0x6000, v2
	global_load_dword v44, v3, s[42:43]
	global_load_dword v45, v3, s[48:49]
	v_add_u32_e32 v3, 0x6800, v2
	global_load_dword v42, v3, s[42:43]
	global_load_dword v43, v3, s[48:49]
	v_add_u32_e32 v3, 0x7000, v2
	global_load_dword v34, v3, s[42:43]
	global_load_dword v35, v3, s[48:49]
	v_add_u32_e32 v2, 0x7800, v2
	global_load_dword v6, v2, s[42:43]
	s_lshl_b32 s1, s0, 2
	global_load_dword v7, v2, s[48:49]
	s_lshl_b32 s12, s46, 2
	v_mov_b32_e32 v2, s1
	global_load_dword v83, v2, s[50:51]
	v_mov_b32_e32 v2, s12
	global_load_dword v84, v2, s[50:51]
	s_mul_i32 s1, s60, s16
	v_readlane_b32 s42, v254, 0
	s_add_i32 s1, s1, s17
	v_readlane_b32 s43, v254, 1
	s_cmp_lt_i32 s1, 0x24000
	s_mov_b64 s[48:49], -1
	s_cbranch_scc1 .LBB0_545
	s_load_dwordx2 s[48:49], s[42:43], 0xd8
	v_mov_b32_e32 v65, v61
	s_waitcnt lgkmcnt(0)
	v_lshl_add_u64 v[4:5], s[48:49], 0, v[64:65]
	s_mov_b64 s[48:49], 0

; __device__ __forceinline__ bool bg_decode(int st, int wg, int NW, int lane, KP kp, const float*& src, int& ldS, bf16_t*& dst, int& o2) {
;     const int g = st * NW + wg;
;     if (g >= BG_STEPS) { src = kp->in[27] + lane; ldS = 0; dst = nullptr; o2 = 0; return false; }
.LBB0_555:
	s_or_b64 exec, exec, s[42:43]
	s_add_i32 s1, s60, 1
	s_mul_i32 s1, s1, s16
	v_readlane_b32 s42, v254, 0
	s_add_i32 s1, s1, s17
	v_mov_b32_e32 v57, v0
	v_readlane_b32 s43, v254, 1
	s_cmp_lt_i32 s1, 0x24000
	s_mov_b64 s[44:45], -1
	s_waitcnt lgkmcnt(0)
	s_barrier
	s_cbranch_scc1 .LBB0_557
	s_load_dwordx2 s[44:45], s[42:43], 0xd8
	v_mov_b32_e32 v65, v61
	s_waitcnt lgkmcnt(0)
	v_lshl_add_u64 v[4:5], s[44:45], 0, v[64:65]
	s_mov_b64 s[44:45], 0

; __device__ __forceinline__ bool bg_decode(int st, int wg, int NW, int lane, KP kp, const float*& src, int& ldS, bf16_t*& dst, int& o2) {
;     const int g = st * NW + wg;
;     if (g >= BG_STEPS) { src = kp->in[27] + lane; ldS = 0; dst = nullptr; o2 = 0; return false; }
.LBB0_569:
	s_or_b64 exec, exec, s[44:45]
	s_add_i32 s1, s60, 2
	s_mul_i32 s1, s1, s16
	v_readlane_b32 s44, v254, 0
	s_add_i32 s1, s1, s17
	v_readlane_b32 s45, v254, 1
	s_cmp_lt_i32 s1, 0x24000
	s_mov_b64 s[48:49], -1
	s_cbranch_scc1 .LBB0_571
	s_load_dwordx2 s[48:49], s[44:45], 0xd8
	v_mov_b32_e32 v65, v61
	s_waitcnt lgkmcnt(0)
	v_lshl_add_u64 v[2:3], s[48:49], 0, v[64:65]
	s_mov_b64 s[48:49], 0

; __device__ __forceinline__ bool bg_decode(int st, int wg, int NW, int lane, KP kp, const float*& src, int& ldS, bf16_t*& dst, int& o2) {
;     const int g = st * NW + wg;
;     if (g >= BG_STEPS) { src = kp->in[27] + lane; ldS = 0; dst = nullptr; o2 = 0; return false; }
.LBB0_581:
	s_or_b64 exec, exec, s[48:49]
	s_add_i32 s1, s60, 3
	s_mul_i32 s1, s1, s16
	v_readlane_b32 s42, v254, 0
	s_add_i32 s1, s1, s17
	v_readlane_b32 s43, v254, 1
	s_cmp_lt_i32 s1, 0x24000
	s_mov_b64 s[48:49], -1
	s_cbranch_scc1 .LBB0_583
	s_load_dwordx2 s[48:49], s[42:43], 0xd8
	v_mov_b32_e32 v65, v61
	s_waitcnt lgkmcnt(0)
	v_lshl_add_u64 v[2:3], s[48:49], 0, v[64:65]
	s_mov_b64 s[48:49], 0

; __device__ __forceinline__ bool bg_decode(int st, int wg, int NW, int lane, KP kp, const float*& src, int& ldS, bf16_t*& dst, int& o2) {
;     const int g = st * NW + wg;
;     if (g >= BG_STEPS) { src = kp->in[27] + lane; ldS = 0; dst = nullptr; o2 = 0; return false; }
.LBB0_593:
	s_or_b64 exec, exec, s[48:49]
	s_add_i32 s1, s60, 4
	s_mul_i32 s1, s1, s16
	v_readlane_b32 s44, v254, 0
	s_add_i32 s1, s1, s17
	v_readlane_b32 s45, v254, 1
	s_cmp_lt_i32 s1, 0x24000
	s_mov_b64 s[48:49], -1
	s_cbranch_scc1 .LBB0_595
	s_load_dwordx2 s[48:49], s[44:45], 0xd8
	v_mov_b32_e32 v65, v61
	s_waitcnt lgkmcnt(0)
	v_lshl_add_u64 v[4:5], s[48:49], 0, v[64:65]
	s_mov_b64 s[48:49], 0

; __device__ __forceinline__ bool bg_decode(int st, int wg, int NW, int lane, KP kp, const float*& src, int& ldS, bf16_t*& dst, int& o2) {
;     const int g = st * NW + wg;
;     if (g >= BG_STEPS) { src = kp->in[27] + lane; ldS = 0; dst = nullptr; o2 = 0; return false; }
.LBB0_608:
	s_or_b64 exec, exec, s[44:45]
	s_add_i32 s1, s60, 5
	s_mul_i32 s1, s1, s16
	v_readlane_b32 s42, v254, 0
	s_add_i32 s1, s1, s17
	v_mov_b32_e32 v6, v0
	v_readlane_b32 s43, v254, 1
	s_cmp_lt_i32 s1, 0x24000
	s_mov_b64 s[44:45], -1
	s_cbranch_scc1 .LBB0_610
	s_load_dwordx2 s[44:45], s[42:43], 0xd8
	v_mov_b32_e32 v65, v61
	s_waitcnt lgkmcnt(0)
	v_lshl_add_u64 v[8:9], s[44:45], 0, v[64:65]
	s_mov_b64 s[44:45], 0

; #define SEG_LD32(dst, off, base) asm volatile("global_load_dword %0, %1, %2" : "=v"(dst) : "v"(off), "s"(base) : "memory")
; #define BG_I(x) bg_issue1<x>(bg, bgwg, bgNW, bglane)
; __device__ __forceinline__ bool bg_decode(int st, int wg, int NW, int lane, KP kp, const float*& src, int& ldS, bf16_t*& dst, int& o2) {
;     const int g = st * NW + wg;
;     if (g >= BG_STEPS) { src = kp->in[27] + lane; ldS = 0; dst = nullptr; o2 = 0; return false; }
; __device__ __forceinline__ void hy_fft_phase(LAS unsigned char* lds, int bid, int G, const bf16_t* vgT, bf16_t* zT, const float* a3, const float* wout, const float* skip, float* filt, float4* gspec) {
;     ...
;             {   unsigned pa[8], pb[8];
; #pragma unroll
;                 for (int i = 0; i < 8; ++i) { const unsigned off = 4u * tid + 2048u * i; SEG_LD32(pa[i], off, v1); SEG_LD32(pb[i], off, v2); }
;                 BG_I(1);
.LBB0_623:
	s_or_b64 exec, exec, s[42:43]
	s_ashr_i32 s1, s0, 31
	s_add_i32 s12, s60, 6
	s_ashr_i32 s47, s46, 31
	s_lshl_b64 s[42:43], s[0:1], 14
	s_add_u32 s42, s64, s42
	s_addc_u32 s43, s65, s43
	s_lshl_b64 s[48:49], s[46:47], 14
	v_mov_b32_e32 v54, v0
	s_add_u32 s48, s64, s48
	s_barrier
	s_addc_u32 s49, s65, s49
	v_lshlrev_b32_e32 v2, 2, v54
	global_load_dword v55, v2, s[42:43]
	global_load_dword v56, v2, s[48:49]
	v_add_u32_e32 v3, 0x800, v2
	global_load_dword v52, v3, s[42:43]
	global_load_dword v53, v3, s[48:49]
	v_add_u32_e32 v3, 0x1000, v2
	global_load_dword v50, v3, s[42:43]
	global_load_dword v51, v3, s[48:49]
	v_add_u32_e32 v3, 0x1800, v2
	global_load_dword v48, v3, s[42:43]
	global_load_dword v49, v3, s[48:49]
	v_add_u32_e32 v3, 0x2000, v2
	global_load_dword v46, v3, s[42:43]
	global_load_dword v47, v3, s[48:49]
	v_add_u32_e32 v3, 0x2800, v2
	global_load_dword v44, v3, s[42:43]
	global_load_dword v45, v3, s[48:49]
	v_add_u32_e32 v3, 0x3000, v2
	global_load_dword v42, v3, s[42:43]
	global_load_dword v43, v3, s[48:49]
	v_add_u32_e32 v2, 0x3800, v2
	global_load_dword v8, v2, s[42:43]
	global_load_dword v9, v2, s[48:49]
	s_mul_i32 s28, s12, s16
	v_readlane_b32 s42, v254, 0
	s_add_i32 s28, s28, s17
	v_readlane_b32 s43, v254, 1
	s_cmp_gt_i32 s28, 0x23fff
	s_mov_b64 s[48:49], -1
	s_cbranch_scc0 .LBB0_625
	s_load_dwordx2 s[48:49], s[42:43], 0xd8
	v_mov_b32_e32 v65, v61
	s_waitcnt lgkmcnt(0)
	v_lshl_add_u64 v[6:7], s[48:49], 0, v[64:65]
	s_mov_b64 s[48:49], 0

; __device__ __forceinline__ bool bg_decode(int st, int wg, int NW, int lane, KP kp, const float*& src, int& ldS, bf16_t*& dst, int& o2) {
;     const int g = st * NW + wg;
;     if (g >= BG_STEPS) { src = kp->in[27] + lane; ldS = 0; dst = nullptr; o2 = 0; return false; }
.LBB0_635:
	s_or_b64 exec, exec, s[46:47]
	s_add_i32 s12, s60, 7
	s_mul_i32 s28, s12, s16
	v_readlane_b32 s44, v254, 0
	s_add_i32 s28, s28, s17
	v_mov_b32_e32 v120, v0
	v_readlane_b32 s45, v254, 1
	s_cmp_lt_i32 s28, 0x24000
	s_mov_b64 s[46:47], -1
	s_waitcnt lgkmcnt(0)
	s_barrier
	s_cbranch_scc1 .LBB0_637
	s_load_dwordx2 s[46:47], s[44:45], 0xd8
	v_mov_b32_e32 v65, v61
	s_waitcnt lgkmcnt(0)
	v_lshl_add_u64 v[4:5], s[46:47], 0, v[64:65]
	s_mov_b64 s[46:47], 0

; __device__ __forceinline__ bool bg_decode(int st, int wg, int NW, int lane, KP kp, const float*& src, int& ldS, bf16_t*& dst, int& o2) {
;     const int g = st * NW + wg;
;     if (g >= BG_STEPS) { src = kp->in[27] + lane; ldS = 0; dst = nullptr; o2 = 0; return false; }
.LBB0_649:
	s_or_b64 exec, exec, s[46:47]
	s_add_i32 s12, s60, 8
	s_mul_i32 s28, s12, s16
	v_readlane_b32 s46, v254, 0
	s_add_i32 s28, s28, s17
	v_readlane_b32 s47, v254, 1
	s_cmp_lt_i32 s28, 0x24000
	s_mov_b64 s[48:49], -1
	s_cbranch_scc1 .LBB0_651
	s_load_dwordx2 s[48:49], s[46:47], 0xd8
	v_mov_b32_e32 v65, v61
	s_waitcnt lgkmcnt(0)
	v_lshl_add_u64 v[2:3], s[48:49], 0, v[64:65]
	s_mov_b64 s[48:49], 0

; __device__ __forceinline__ bool bg_decode(int st, int wg, int NW, int lane, KP kp, const float*& src, int& ldS, bf16_t*& dst, int& o2) {
;     const int g = st * NW + wg;
;     if (g >= BG_STEPS) { src = kp->in[27] + lane; ldS = 0; dst = nullptr; o2 = 0; return false; }
.LBB0_661:
	s_or_b64 exec, exec, s[48:49]
	s_add_i32 s12, s60, 9
	s_mul_i32 s28, s12, s16
	v_readlane_b32 s44, v254, 0
	s_add_i32 s28, s28, s17
	v_readlane_b32 s45, v254, 1
	s_cmp_lt_i32 s28, 0x24000
	s_mov_b64 s[48:49], -1
	s_cbranch_scc1 .LBB0_663
	s_load_dwordx2 s[48:49], s[44:45], 0xd8
	v_mov_b32_e32 v65, v61
	s_waitcnt lgkmcnt(0)
	v_lshl_add_u64 v[2:3], s[48:49], 0, v[64:65]
	s_mov_b64 s[48:49], 0

; __device__ __forceinline__ bool bg_decode(int st, int wg, int NW, int lane, KP kp, const float*& src, int& ldS, bf16_t*& dst, int& o2) {
;     const int g = st * NW + wg;
;     if (g >= BG_STEPS) { src = kp->in[27] + lane; ldS = 0; dst = nullptr; o2 = 0; return false; }
.LBB0_673:
	s_or_b64 exec, exec, s[44:45]
	s_add_i32 s12, s60, 10
	s_mul_i32 s28, s12, s16
	v_readlane_b32 s44, v254, 0
	s_add_i32 s28, s28, s17
	v_readlane_b32 s45, v254, 1
	s_cmp_lt_i32 s28, 0x24000
	s_mov_b64 s[46:47], -1
	s_cbranch_scc1 .LBB0_675
	s_load_dwordx2 s[46:47], s[44:45], 0xd8
	v_mov_b32_e32 v65, v61
	s_waitcnt lgkmcnt(0)
	v_lshl_add_u64 v[4:5], s[46:47], 0, v[64:65]
	s_mov_b64 s[46:47], 0

; #define SEG_LD64(dst, off, base) asm volatile("global_load_dwordx2 %0, %1, %2" : "=v"(dst) : "v"(off), "s"(base) : "memory")
; #define BG_I(x) bg_issue1<x>(bg, bgwg, bgNW, bglane)
; __device__ __forceinline__ bool bg_decode(int st, int wg, int NW, int lane, KP kp, const float*& src, int& ldS, bf16_t*& dst, int& o2) {
;     const int g = st * NW + wg;
;     if (g >= BG_STEPS) { src = kp->in[27] + lane; ldS = 0; dst = nullptr; o2 = 0; return false; }
; __device__ __forceinline__ void hy_fft_phase(LAS unsigned char* lds, int bid, int G, const bf16_t* vgT, bf16_t* zT, const float* a3, const float* wout, const float* skip, float* filt, float4* gspec) {
;     ...
;             {   u32x2 gq[16], gh;
; #pragma unroll
;                 for (int i = 0; i < 16; ++i) { const unsigned off = 8u * tid + 4096u * i; SEG_LD64(gq[i], off, GS); }
;                 { const unsigned off = 8u * (FN / 2); SEG_LD64(gh, off, GS); }
;                 BG_I(0);
.LBB0_688:
	s_or_b64 exec, exec, s[46:47]
	v_mov_b32_e32 v114, v0
	s_add_i32 s12, s60, 11
	v_lshlrev_b32_e32 v4, 3, v114
	global_load_dwordx2 v[38:39], v4, s[20:21]
	v_add_u32_e32 v5, 0x1000, v4
	global_load_dwordx2 v[36:37], v5, s[20:21]
	v_add_u32_e32 v5, 0x2000, v4
	global_load_dwordx2 v[34:35], v5, s[20:21]
	v_add_u32_e32 v5, 0x3000, v4
	global_load_dwordx2 v[32:33], v5, s[20:21]
	v_add_u32_e32 v5, 0x4000, v4
	global_load_dwordx2 v[30:31], v5, s[20:21]
	v_add_u32_e32 v5, 0x5000, v4
	global_load_dwordx2 v[28:29], v5, s[20:21]
	v_add_u32_e32 v5, 0x6000, v4
	global_load_dwordx2 v[26:27], v5, s[20:21]
	v_add_u32_e32 v5, 0x7000, v4
	global_load_dwordx2 v[24:25], v5, s[20:21]
	v_add_u32_e32 v5, 0x8000, v4
	global_load_dwordx2 v[22:23], v5, s[20:21]
	v_add_u32_e32 v5, 0x9000, v4
	global_load_dwordx2 v[20:21], v5, s[20:21]
	v_add_u32_e32 v5, 0xa000, v4
	global_load_dwordx2 v[18:19], v5, s[20:21]
	v_add_u32_e32 v5, 0xb000, v4
	global_load_dwordx2 v[16:17], v5, s[20:21]
	v_add_u32_e32 v5, 0xc000, v4
	global_load_dwordx2 v[14:15], v5, s[20:21]
	v_add_u32_e32 v5, 0xd000, v4
	global_load_dwordx2 v[12:13], v5, s[20:21]
	v_add_u32_e32 v5, 0xe000, v4
	global_load_dwordx2 v[10:11], v5, s[20:21]
	v_add_u32_e32 v4, 0xf000, v4
	global_load_dwordx2 v[8:9], v4, s[20:21]
	global_load_dwordx2 v[6:7], v119, s[20:21]
	s_mul_i32 s28, s12, s16
	v_readlane_b32 s46, v254, 0
	s_add_i32 s28, s28, s17
	v_readlane_b32 s47, v254, 1
	s_cmp_lt_i32 s28, 0x24000
	s_mov_b64 s[48:49], -1
	s_cbranch_scc1 .LBB0_690
	s_load_dwordx2 s[48:49], s[46:47], 0xd8
	v_mov_b32_e32 v65, v61
	s_waitcnt lgkmcnt(0)
	v_lshl_add_u64 v[40:41], s[48:49], 0, v[64:65]
	s_mov_b64 s[48:49], 0

; __device__ __forceinline__ bool bg_decode(int st, int wg, int NW, int lane, KP kp, const float*& src, int& ldS, bf16_t*& dst, int& o2) {
;     const int g = st * NW + wg;
;     if (g >= BG_STEPS) { src = kp->in[27] + lane; ldS = 0; dst = nullptr; o2 = 0; return false; }
.LBB0_702:
	s_or_b64 exec, exec, s[48:49]
	s_add_i32 s12, s60, 12
	s_mul_i32 s28, s12, s16
	v_readlane_b32 s44, v254, 0
	s_add_i32 s28, s28, s17
	v_mov_b32_e32 v128, v0
	v_readlane_b32 s45, v254, 1
	s_cmp_lt_i32 s28, 0x24000
	s_mov_b64 s[48:49], -1
	s_waitcnt lgkmcnt(0)
	s_barrier
	s_cbranch_scc1 .LBB0_704
	s_load_dwordx2 s[48:49], s[44:45], 0xd8
	v_mov_b32_e32 v65, v61
	s_waitcnt lgkmcnt(0)
	v_lshl_add_u64 v[2:3], s[48:49], 0, v[64:65]
	s_mov_b64 s[48:49], 0

; __device__ __forceinline__ bool bg_decode(int st, int wg, int NW, int lane, KP kp, const float*& src, int& ldS, bf16_t*& dst, int& o2) {
;     const int g = st * NW + wg;
;     if (g >= BG_STEPS) { src = kp->in[27] + lane; ldS = 0; dst = nullptr; o2 = 0; return false; }
.LBB0_717:
	s_or_b64 exec, exec, s[44:45]
	s_add_i32 s12, s60, 13
	s_mul_i32 s28, s12, s16
	v_readlane_b32 s44, v254, 0
	s_add_i32 s28, s28, s17
	v_readlane_b32 s45, v254, 1
	s_cmp_lt_i32 s28, 0x24000
	s_mov_b64 s[46:47], -1
	s_cbranch_scc1 .LBB0_719
	s_load_dwordx2 s[46:47], s[44:45], 0xd8
	v_mov_b32_e32 v65, v61
	s_waitcnt lgkmcnt(0)
	v_lshl_add_u64 v[2:3], s[46:47], 0, v[64:65]
	s_mov_b64 s[46:47], 0

; __device__ __forceinline__ bool bg_decode(int st, int wg, int NW, int lane, KP kp, const float*& src, int& ldS, bf16_t*& dst, int& o2) {
;     const int g = st * NW + wg;
;     if (g >= BG_STEPS) { src = kp->in[27] + lane; ldS = 0; dst = nullptr; o2 = 0; return false; }
.LBB0_729:
	s_or_b64 exec, exec, s[46:47]
	s_add_i32 s12, s60, 14
	s_mul_i32 s28, s12, s16
	v_readlane_b32 s46, v254, 0
	s_add_i32 s28, s28, s17
	v_readlane_b32 s47, v254, 1
	s_cmp_lt_i32 s28, 0x24000
	s_mov_b64 s[48:49], -1
	s_cbranch_scc1 .LBB0_731
	s_load_dwordx2 s[48:49], s[46:47], 0xd8
	v_mov_b32_e32 v65, v61
	s_waitcnt lgkmcnt(0)
	v_lshl_add_u64 v[2:3], s[48:49], 0, v[64:65]
	s_mov_b64 s[48:49], 0

; __device__ __forceinline__ bool bg_decode(int st, int wg, int NW, int lane, KP kp, const float*& src, int& ldS, bf16_t*& dst, int& o2) {
;     const int g = st * NW + wg;
;     if (g >= BG_STEPS) { src = kp->in[27] + lane; ldS = 0; dst = nullptr; o2 = 0; return false; }
.LBB0_741:
	s_or_b64 exec, exec, s[48:49]
	s_add_i32 s12, s60, 15
	s_mul_i32 s28, s12, s16
	v_readlane_b32 s44, v254, 0
	s_add_i32 s28, s28, s17
	v_readlane_b32 s45, v254, 1
	s_cmp_lt_i32 s28, 0x24000
	s_mov_b64 s[48:49], -1
	s_cbranch_scc1 .LBB0_743
	s_load_dwordx2 s[48:49], s[44:45], 0xd8
	v_mov_b32_e32 v65, v61
	s_waitcnt lgkmcnt(0)
	v_lshl_add_u64 v[2:3], s[48:49], 0, v[64:65]
	s_mov_b64 s[48:49], 0

; #define BG_I(x) bg_issue1<x>(bg, bgwg, bgNW, bglane)
; __device__ __forceinline__ bool bg_decode(int st, int wg, int NW, int lane, KP kp, const float*& src, int& ldS, bf16_t*& dst, int& o2) {
;     const int g = st * NW + wg;
;     if (g >= BG_STEPS) { src = kp->in[27] + lane; ldS = 0; dst = nullptr; o2 = 0; return false; }
; __device__ __forceinline__ void hy_fft_phase(LAS unsigned char* lds, int bid, int G, const bf16_t* vgT, bf16_t* zT, const float* a3, const float* wout, const float* skip, float* filt, float4* gspec) {
;     ...
;     { const int nst = (BG_STEPS + bgNW - 1) / bgNW;
;       if (bg.st < nst) { BG_I(0);
.LBB0_775:
	s_abs_i32 s0, s16
	v_cvt_f32_u32_e32 v1, s0
	s_sub_i32 s3, 0, s0
	s_add_i32 s1, s16, 0x23fff
	s_xor_b32 s2, s1, s16
	v_rcp_iflag_f32_e32 v1, v1
	s_abs_i32 s1, s1
	s_ashr_i32 s2, s2, 31
	v_mul_f32_e32 v1, 0x4f7ffffe, v1
	v_cvt_u32_f32_e32 v1, v1
	s_nop 0
	v_readfirstlane_b32 s4, v1
	s_mul_i32 s3, s3, s4
	s_mul_hi_u32 s3, s4, s3
	s_add_i32 s4, s4, s3
	s_mul_hi_u32 s3, s1, s4
	s_mul_i32 s4, s3, s0
	s_sub_i32 s1, s1, s4
	s_add_i32 s5, s3, 1
	s_sub_i32 s4, s1, s0
	s_cmp_ge_u32 s1, s0
	s_cselect_b32 s3, s5, s3
	s_cselect_b32 s1, s4, s1
	s_add_i32 s4, s3, 1
	s_cmp_ge_u32 s1, s0
	s_cselect_b32 s0, s4, s3
	s_xor_b32 s0, s0, s2
	s_sub_i32 s12, s0, s2
	s_cmp_lt_i32 s60, s12
	s_cbranch_scc0 .LBB0_816
	s_mul_i32 s6, s60, s16
	v_readlane_b32 s0, v254, 0
	s_add_i32 s6, s6, s17
	v_readlane_b32 s1, v254, 1
	s_cmp_lt_i32 s6, 0x24000
	s_cbranch_scc1 .LBB0_779
	s_load_dwordx2 s[2:3], s[0:1], 0xd8
	v_lshlrev_b32_e32 v2, 2, v58
	v_mov_b32_e32 v3, 0
	s_waitcnt lgkmcnt(0)
	v_lshl_add_u64 v[4:5], s[2:3], 0, v[2:3]
	s_cbranch_execz .LBB0_780
	s_mov_b64 s[2:3], 0
	v_mov_b64_e32 v[2:3], 0
	s_mov_b32 s0, 0
	s_branch .LBB0_786

; __device__ __forceinline__ bool bg_decode(int st, int wg, int NW, int lane, KP kp, const float*& src, int& ldS, bf16_t*& dst, int& o2) {
;     const int g = st * NW + wg;
;     if (g >= BG_STEPS) { src = kp->in[27] + lane; ldS = 0; dst = nullptr; o2 = 0; return false; }
;     const int l = g / 98304, r = g - l * 98304;
;     unsigned char* ws = kp->ws;
.LBB0_789:
	v_readlane_b32 s6, v254, 0
	s_add_i32 s1, s14, s17
	v_readlane_b32 s7, v254, 1
	s_mov_b64 s[8:9], -1
	s_cmp_lt_i32 s1, 0x24000
	v_lshlrev_b32_e32 v12, 2, v58
	s_cbranch_scc1 .LBB0_791
	s_load_dwordx2 s[8:9], s[6:7], 0xd8
	v_mov_b32_e32 v13, v5
	s_waitcnt lgkmcnt(0)
	v_lshl_add_u64 v[14:15], s[8:9], 0, v[12:13]
	s_mov_b64 s[8:9], 0

; __device__ __forceinline__ bool bg_decode(int st, int wg, int NW, int lane, KP kp, const float*& src, int& ldS, bf16_t*& dst, int& o2) {
;     const int g = st * NW + wg;
;     if (g >= BG_STEPS) { src = kp->in[27] + lane; ldS = 0; dst = nullptr; o2 = 0; return false; }
;     const int l = g / 98304, r = g - l * 98304;
;     unsigned char* ws = kp->ws;
.LBB0_801:
	s_or_b64 exec, exec, s[8:9]
	v_readlane_b32 s0, v254, 0
	s_add_i32 s7, s22, s17
	v_readlane_b32 s1, v254, 1
	s_cmp_lt_i32 s7, 0x24000
	s_mov_b64 s[8:9], -1
	s_cbranch_scc1 .LBB0_803
	s_load_dwordx2 s[8:9], s[0:1], 0xd8
	v_mov_b32_e32 v13, v5
	s_waitcnt lgkmcnt(0)
	v_lshl_add_u64 v[14:15], s[8:9], 0, v[12:13]
	s_mov_b64 s[8:9], 0

; __device__ __forceinline__ int tid_fresh() { int t = threadIdx.x; asm volatile("" : "+v"(t)); return t; }
;     __device__ __forceinline__ const char* a_base() const { return (const char*)A; }
; template <class Epi, class Sched>
; __device__ __forceinline__ void gemm_phase(LAS unsigned char* lds, const int K, const Sched& S, const Epi& E) {
;     const int tid = tid_fresh(), wid = __builtin_amdgcn_readfirstlane(tid >> 6), lane = tid & 63, wr = wid >> 2, wc = wid & 3, fr = lane & 15, fq = lane >> 4;
;     const int nt = K / BK;
;     int R0, C0, R1, C1; stage_rc(tid * 16, R0, C0); stage_rc(tid * 16 + 8192, R1, C1);
;     const int Rb0 = Epi::PERM ? ((R0 & ~31) + perm32(R0 & 31)) : R0, Rb1 = Epi::PERM ? ((R1 & ~31) + perm32(R1 & 31)) : R1;
;     const unsigned voffB0 = S.b_off(Rb0, C0), voffB1 = S.b_off(Rb1, C1);
;     __device__ __forceinline__ bool next(int i, Unit& u) const {
;         const int L = i * G + c; if (L >= ntiles * 4) return false;
;         const int rt = L >> 2; u.pn = L & 3; u.e = tile_e[rt]; u.pm = rt - tstart[u.e]; u.rbase = (u.e < NE) ? rt * BM : SLOT_SH + u.pm * BM; return true;
;     }
;     __device__ __forceinline__ const char* a_base() const { return (const char*)A; }
;     __device__ __forceinline__ unsigned a_off(const Unit& u, int r) const {
;         const int pos = u.pm * BM + r; int tok = pos;
;         if (u.e < NE) { tok = 0; if (pos < cnt[u.e]) tok = list[u.e * T + pos]; }
;         return (unsigned)tok * (unsigned)(D * 2);
;     }
;     __device__ __forceinline__ void a_off4(const Unit& u, int r0, int r1, unsigned& o00, unsigned& o01, unsigned& o10, unsigned& o11) const {
;         const int p0 = u.pm * BM + r0, p1 = u.pm * BM + r1, p2 = p0 + HALF, p3 = p1 + HALF;
;         if (u.e >= NE) { o00 = (unsigned)p0 * (unsigned)(D * 2); o01 = (unsigned)p1 * (unsigned)(D * 2); o10 = (unsigned)p2 * (unsigned)(D * 2); o11 = (unsigned)p3 * (unsigned)(D * 2); return; }
;         const int* lp = list + u.e * T;
;         int v0 = lp[p0], v1 = lp[p1], v2 = lp[p2], v3 = lp[p3];
;         asm volatile("" : "+v"(v0), "+v"(v1), "+v"(v2), "+v"(v3));
;         const int c = cnt[u.e];
;         o00 = p0 < c ? (unsigned)v0 * (unsigned)(D * 2) : 0u; o01 = p1 < c ? (unsigned)v1 * (unsigned)(D * 2) : 0u;
;         o10 = p2 < c ? (unsigned)v2 * (unsigned)(D * 2) : 0u; o11 = p3 < c ? (unsigned)v3 * (unsigned)(D * 2) : 0u;
.LBB0_1077:
	s_or_b64 exec, exec, s[0:1]
	v_readlane_b32 s2, v254, 5
	v_readlane_b32 s0, v254, 0
	s_and_b32 s3, s2, 3
	v_readlane_b32 s1, v254, 1
	s_lshl_b32 s29, s28, 2
	v_writelane_b32 v254, s3, 27
	s_lshl_b32 s3, s3, 12
	v_mov_b32_e32 v6, v0
	s_waitcnt lgkmcnt(0)
	s_barrier
	v_readlane_b32 s84, v254, 0
	v_readlane_b32 s85, v254, 1
	s_nop 1
	s_load_dwordx2 s[74:75], s[84:85], 0xd8
	s_load_dwordx2 s[76:77], s[84:85], 0xe0
	s_load_dwordx2 s[78:79], s[84:85], 0x118
	v_and_b32_e32 v252, 63, v0
	v_lshrrev_b32_e32 v253, 6, v0
	v_lshlrev_b32_e32 v238, 2, v252
	v_lshlrev_b32_e32 v252, 4, v252
	v_add_u32_e32 v239, 0x800, v238
	v_add_u32_e32 v240, 0x1000, v238
	v_add_u32_e32 v241, 0x1800, v238
	v_readlane_b32 s86, v254, 4
	v_readlane_b32 s87, v255, 40
	v_readfirstlane_b32 s88, v253
	s_nop 3
	s_lshl_b32 s71, s86, 3
	s_lshl_b32 s87, s87, 3
	s_add_u32 s87, s87, s88
	s_add_u32 s70, s87, 0x24000
	s_mov_b32 s80, 0
	s_mov_b32 s82, 0
	s_mov_b32 s90, 0
	s_waitcnt lgkmcnt(0)
	v_writelane_b32 v255, s3, 24
	s_cmp_lt_i32 s2, s29
	s_nop 0
	v_readfirstlane_b32 s30, v6
	s_cbranch_scc0 .LBB0_1099
	v_ashrrev_i32_e32 v1, 31, v6
	v_lshrrev_b32_e32 v1, 26, v1
	v_add_u32_e32 v1, v6, v1
	v_ashrrev_i32_e32 v9, 6, v1
	v_bfe_i32 v1, v6, 27, 1
	v_lshlrev_b32_e32 v2, 4, v6
	v_lshrrev_b32_e32 v1, 22, v1
	v_add_u32_e32 v1, v2, v1
	v_and_b32_e32 v1, 0xfffffc00, v1
	v_sub_u32_e32 v1, v2, v1
	v_lshrrev_b32_e32 v3, 4, v1
	v_bitop3_b32 v10, v3, v1, 32 bitop3:0x6c
	v_ashrrev_i32_e32 v1, 31, v1
	v_lshrrev_b32_e32 v1, 26, v1
	s_load_dwordx2 s[0:1], s[0:1], 0x118
	v_lshlrev_b32_e32 v3, 3, v9
	v_add_u32_e32 v1, v10, v1
	v_and_b32_e32 v3, -16, v3
	v_ashrrev_i32_e32 v8, 6, v1
	v_add_u32_e32 v2, 0x2000, v2
	v_add_u32_e32 v1, v8, v3
	v_ashrrev_i32_e32 v3, 31, v2
	v_lshrrev_b32_e32 v3, 22, v3
	v_add_u32_e32 v3, v2, v3
	s_waitcnt lgkmcnt(0)
	s_add_u32 s31, s0, 0x3ec30000
	v_ashrrev_i32_e32 v11, 10, v3
	v_readlane_b32 s3, v254, 5
	s_addc_u32 s33, s1, 0
	v_mul_i32_i24_e32 v3, 0x400, v11
	s_and_b32 s2, s3, -4
	v_sub_u32_e32 v2, v2, v3
	s_add_i32 s2, s2, 0
	v_lshrrev_b32_e32 v3, 4, v2
	s_add_i32 s2, s2, 0x21160
	v_bitop3_b32 v12, v3, v2, 32 bitop3:0x6c
	v_mov_b32_e32 v3, s2
	ds_read_b32 v3, v3
	v_ashrrev_i32_e32 v4, 31, v12
	v_lshrrev_b32_e32 v4, 26, v4
	v_lshlrev_b32_e32 v2, 3, v11
	v_add_u32_e32 v4, v12, v4
	s_waitcnt lgkmcnt(0)
	v_lshlrev_b32_e32 v5, 2, v3
	v_add_u32_e32 v5, 0, v5
	v_add_u32_e32 v5, 0x21040, v5
	ds_read_b32 v5, v5
	v_and_b32_e32 v2, -16, v2
	v_ashrrev_i32_e32 v13, 6, v4
	s_ashr_i32 s8, s3, 2
	v_add_u32_e32 v146, v13, v2
	s_waitcnt lgkmcnt(0)
	v_sub_u32_e32 v2, s8, v5
	v_lshlrev_b32_e32 v7, 8, v2
	v_add_u32_e32 v2, v7, v1
	v_add_u32_e32 v4, v7, v146
	v_cmp_gt_i32_e32 vcc, 64, v3
	v_readfirstlane_b32 s6, v3
	v_add_u32_e32 v14, 0x80, v2
	v_add_u32_e32 v15, 0x80, v4
	s_cbranch_vccz .LBB0_1080
	s_lshl_b32 s2, s6, 13
	s_ashr_i32 s3, s2, 31
	s_lshl_b64 s[2:3], s[2:3], 2
	s_add_u32 s2, s31, s2
	s_addc_u32 s3, s33, s3
	v_ashrrev_i32_e32 v3, 31, v2
	v_lshl_add_u64 v[16:17], v[2:3], 2, s[2:3]
	v_ashrrev_i32_e32 v5, 31, v4
	v_lshl_add_u64 v[18:19], v[4:5], 2, s[2:3]
	global_load_dword v3, v[16:17], off
	global_load_dword v5, v[18:19], off
	global_load_dword v20, v[18:19], off offset:512
	global_load_dword v21, v[16:17], off offset:512
	s_lshl_b32 s2, s6, 2
	s_add_i32 s2, s2, 0
	s_add_i32 s2, s2, 0x21660
	v_mov_b32_e32 v16, s2
	s_waitcnt vmcnt(0)
	ds_read_b32 v17, v16
	v_lshlrev_b32_e32 v3, 12, v3
	v_lshlrev_b32_e32 v5, 12, v5
	v_lshlrev_b32_e32 v16, 12, v21
	v_lshlrev_b32_e32 v18, 12, v20
	s_waitcnt lgkmcnt(0)
	v_cmp_lt_i32_e32 vcc, v2, v17
	s_nop 1
	v_cndmask_b32_e32 v3, 0, v3, vcc
	v_cmp_lt_i32_e32 vcc, v4, v17
	s_nop 1
	v_cndmask_b32_e32 v5, 0, v5, vcc
	v_cmp_lt_i32_e32 vcc, v14, v17
	s_nop 1
	v_cndmask_b32_e32 v16, 0, v16, vcc
	v_cmp_lt_i32_e32 vcc, v15, v17
	s_nop 1
	v_cndmask_b32_e32 v17, 0, v18, vcc
	s_cbranch_execz .LBB0_1081
	s_branch .LBB0_1082

; #define PG8_STAGE(bufoff, gbase, v0, v1) do { \
;         __builtin_amdgcn_global_load_lds((const unsigned*)((const char*)(gbase) + (v0)), (LAS unsigned*)(lds + (bufoff) + ldsw), 16, 0, 0); \
;         __builtin_amdgcn_global_load_lds((const unsigned*)((const char*)(gbase) + (v1)), (LAS unsigned*)(lds + (bufoff) + ldsw + 8192), 16, 0, 0); } while (0)
; #define PG8_LDA(dst, b, h) do { _Pragma("unroll") for (int m = 0; m < 4; ++m) _Pragma("unroll") for (int k = 0; k < 2; ++k) dst[m][k] = *(const LAS bf16x8*)(lds + PG8_SA(b, h) + aoff + m * 2048 + k * 1024); } while (0)
; #define PG8_LDB(dst, b, h) do { _Pragma("unroll") for (int n = 0; n < 2; ++n) _Pragma("unroll") for (int k = 0; k < 2; ++k) dst[n][k] = *(const LAS bf16x8*)(lds + PG8_SB(b, h) + boff + n * 2048 + k * 1024); } while (0)
; #define PG8_MMA(ai, bj, At, Bt) do { __builtin_amdgcn_s_setprio(1); _Pragma("unroll") for (int m = 0; m < 4; ++m) _Pragma("unroll") for (int n = 0; n < 2; ++n) _Pragma("unroll") for (int k = 0; k < 2; ++k) \
;         acc[ai][bj][m][n] = __builtin_amdgcn_mfma_f32_16x16x32_bf16(Bt[n][k], At[m][k], acc[ai][bj][m][n], 0, 0, 0); __builtin_amdgcn_s_setprio(0); } while (0)
; #define PG8_WAIT_V(n) asm volatile("s_waitcnt vmcnt(" #n ")" ::: "memory")
; #define PG8_BAR __builtin_amdgcn_s_barrier()
; #define PG8_SCHED __builtin_amdgcn_sched_barrier(0)
; template <class Epi, class Sched>
; __device__ __forceinline__ void gemm_phase(LAS unsigned char* lds, const int K, const Sched& S, const Epi& E) {
;     ...
;             PG8_WAIT_V(6); PG8_BAR; PG8_MMA(1, 1, At, B1); PG8_BAR;
;             PG8_LDB(B0, 1, 0); PG8_SCHED; PG8_LDA(At, 1, 0); PG8_STAGE(PG8_SA(0, 1), a2, x10, x11);
; __device__ __forceinline__ bool bg_decode(int st, int wg, int NW, int lane, KP kp, const float*& src, int& ldS, bf16_t*& dst, int& o2) {
;     ...
;     if (r < 65536) {
;         const int e = r >> 10, kc = (r >> 2) & 255, kind = (r >> 1) & 1, cc = r & 1, n = cc * 256 + lane;
;         ldS = FF; o2 = 256 * 8;
;         src = kp->in[27 + kind] + ((size_t)(l * NE + e) * D + kc * 8) * FF + n;
;         const int drow = (n >> 7) * 256 + kind * 128 + (n & 127);
;         dst = (bf16_t*)(ws + WS_WGU) + l * WGU_L + (size_t)e * 1024 * D + ((size_t)kc * 1024 + drow) * 8;
.Lpb8_p4j:
	s_barrier
	s_setprio 1
	v_mfma_f32_16x16x32_bf16 v[54:57], v[212:215], v[176:179], v[54:57]
	v_mfma_f32_16x16x32_bf16 v[50:53], v[220:223], v[176:179], v[50:53]
	v_mfma_f32_16x16x32_bf16 v[38:41], v[212:215], v[184:187], v[38:41]
	v_mfma_f32_16x16x32_bf16 v[34:37], v[220:223], v[184:187], v[34:37]
	v_mfma_f32_16x16x32_bf16 v[22:25], v[212:215], v[192:195], v[22:25]
	v_mfma_f32_16x16x32_bf16 v[18:21], v[220:223], v[192:195], v[18:21]
	v_mfma_f32_16x16x32_bf16 v[6:9], v[212:215], v[200:203], v[6:9]
	v_mfma_f32_16x16x32_bf16 v[2:5], v[220:223], v[200:203], v[2:5]
	v_mfma_f32_16x16x32_bf16 v[54:57], v[216:219], v[180:183], v[54:57]
	v_mfma_f32_16x16x32_bf16 v[50:53], v[224:227], v[180:183], v[50:53]
	v_mfma_f32_16x16x32_bf16 v[38:41], v[216:219], v[188:191], v[38:41]
	v_mfma_f32_16x16x32_bf16 v[34:37], v[224:227], v[188:191], v[34:37]
	v_mfma_f32_16x16x32_bf16 v[22:25], v[216:219], v[196:199], v[22:25]
	v_mfma_f32_16x16x32_bf16 v[18:21], v[224:227], v[196:199], v[18:21]
	v_mfma_f32_16x16x32_bf16 v[6:9], v[216:219], v[208:211], v[6:9]
	v_mfma_f32_16x16x32_bf16 v[2:5], v[224:227], v[208:211], v[2:5]
	s_setprio 0
	s_add_i32 s55, 0, 0x18000
	v_add_u32_e32 v134, s55, v149
	s_barrier
	ds_read_b128 v[160:163], v134
	ds_read_b128 v[164:167], v134 offset:1024
	ds_read_b128 v[168:171], v134 offset:2048
	ds_read_b128 v[172:175], v134 offset:3072
	s_mov_b32 m0, s39
	ds_read_b128 v[176:179], v151 offset:32768
	ds_read_b128 v[180:183], v151 offset:33792
	ds_read_b128 v[184:187], v151 offset:34816
	ds_read_b128 v[188:191], v151 offset:35840
	ds_read_b128 v[192:195], v151 offset:36864
	ds_read_b128 v[196:199], v151 offset:37888
	ds_read_b128 v[200:203], v151 offset:38912
	ds_read_b128 v[208:211], v151 offset:39936
	v_cndmask_b32_e32 v134, v140, v153, vcc
	global_load_lds_dwordx4 v139, s[26:27]
	s_mov_b32 m0, s40
	s_nop 0
	global_load_lds_dwordx4 v134, s[26:27]
	s_add_u32 s90, s90, 1
	s_cmp_lt_u32 s90, 2
	s_cbranch_scc1 .Lpb8_p5n
	s_mov_b32 s90, 0
	s_cmp_ge_u32 s70, 0x28000
	s_cbranch_scc1 .Lpb8_p5n
	s_cmp_eq_u32 s80, 0
	s_cbranch_scc0 .Lpb8_adv2
	s_cmp_ge_u32 s70, 0x18000
	s_cselect_b32 s84, 0x18000, 0
	s_cselect_b32 s83, 0x10000000, 0
	s_mov_b32 s81, 0x4030000
	s_cselect_b32 s81, 0x14430000, s81
	s_sub_u32 s84, s70, s84
	s_lshr_b32 s85, s84, 2
	s_lshl_b32 s85, s85, 14
	s_and_b32 s86, s84, 1
	s_lshl_b32 s87, s86, 10
	s_add_u32 s87, s87, s85
	s_add_u32 s87, s87, s83
	s_bitcmp1_b32 s84, 1
	s_cselect_b64 s[72:73], s[76:77], s[74:75]
	s_add_u32 s72, s72, s87
	s_addc_u32 s73, s73, 0
	s_add_u32 s88, s72, 0x2000
	s_addc_u32 s89, s73, 0
	s_lshl_b32 s86, s86, 13
	s_add_u32 s85, s85, s86
	s_and_b32 s86, s84, 2
	s_lshl_b32 s86, s86, 10
	s_add_u32 s85, s85, s86
	s_add_u32 s85, s85, s81
	v_add_u32_e32 v253, s85, v252
	s_movk_i32 s81, 0x400
	s_branch .Lpb8_ld2
